# speedup vs baseline: 1.0209x; 1.0039x over previous
_Z9ssim_mainPKfS0_S0_Pf:
	v_readfirstlane_b32 s29, v0
	s_load_dwordx4 s[4:7], s[0:1], 0x0
	s_load_dwordx4 s[8:11], s[0:1], 0x10
	s_mov_b32 s51, 0x44800000
	s_mov_b32 s38, 0
	s_mov_b32 s39, -1
	s_lshr_b32 s12, s29, 6
	s_mov_b32 s13, s2
	s_lshr_b32 s14, s13, 3
	s_and_b32 s15, s13, 7
	s_lshl_b32 s16, s14, 20
	s_lshl_b32 s17, s15, 17
	s_add_u32 s16, s16, s17
	s_lshl_b32 s17, s12, 8
	s_add_u32 s16, s16, s17
	s_lshl_b32 s27, s12, 2
	s_add_u32 s27, s27, 0x10000
	v_and_b32_e32 v8, 63, v0
	v_and_b32_e32 v169, 15, v0
	v_bfe_u32 v164, v0, 4, 2
	v_lshrrev_b32_e32 v167, 2, v169
	v_lshlrev_b32_e32 v167, 5, v167
	v_and_b32_e32 v168, 1, v169
	v_lshl_or_b32 v167, v168, 4, v167
	v_bfe_u32 v168, v169, 1, 1
	v_lshl_or_b32 v167, v168, 7, v167
	v_lshl_or_b32 v9, v164, 14, v167
	v_and_b32_e32 v168, 1, v164
	v_lshl_or_b32 v23, v168, 14, v167
	v_lshrrev_b32_e32 v168, 1, v164
	v_lshl_or_b32 v23, v168, 13, v23
	v_add_u32_e32 v237, 0x1000, v9
	v_add_u32_e32 v238, 0x2000, v9
	v_add_u32_e32 v239, 0x3000, v9
	v_add_u32_e32 v240, 0x10000, v9
	v_add_u32_e32 v241, 0x11000, v9
	v_add_u32_e32 v242, 0x12000, v9
	v_add_u32_e32 v243, 0x13000, v9
	s_waitcnt lgkmcnt(0)
	s_load_dwordx8 s[40:47], s[8:9], 0x0
	s_load_dwordx2 s[48:49], s[8:9], 0x20
	s_load_dword s50, s[8:9], 0x28
	s_add_u32 s18, s4, s16
	s_addc_u32 s19, s5, 0
	s_add_u32 s20, s6, s16
	s_addc_u32 s21, s7, 0
	global_load_dwordx4 v[36:39], v9, s[18:19] offset:0 nt
	global_load_dwordx4 v[40:43], v9, s[18:19] offset:2048 nt
	global_load_dwordx4 v[68:71], v9, s[20:21] offset:0 nt
	global_load_dwordx4 v[72:75], v9, s[20:21] offset:2048 nt
	global_load_dwordx4 v[44:47], v237, s[18:19] offset:0 nt
	global_load_dwordx4 v[48:51], v237, s[18:19] offset:2048 nt
	global_load_dwordx4 v[76:79], v237, s[20:21] offset:0 nt
	global_load_dwordx4 v[80:83], v237, s[20:21] offset:2048 nt
	global_load_dwordx4 v[52:55], v238, s[18:19] offset:0 nt
	global_load_dwordx4 v[56:59], v238, s[18:19] offset:2048 nt
	global_load_dwordx4 v[84:87], v238, s[20:21] offset:0 nt
	global_load_dwordx4 v[88:91], v238, s[20:21] offset:2048 nt
	global_load_dwordx4 v[60:63], v239, s[18:19] offset:0 nt
	global_load_dwordx4 v[64:67], v239, s[18:19] offset:2048 nt
	global_load_dwordx4 v[92:95], v239, s[20:21] offset:0 nt
	global_load_dwordx4 v[96:99], v239, s[20:21] offset:2048 nt
	v_mov_b32_e32 v6, s27
	v_mov_b32_e32 v168, 0
	ds_write_b32 v6, v168 offset:0
	ds_write_b32 v6, v168 offset:32
	ds_write_b32 v6, v168 offset:64
	ds_write_b32 v6, v168 offset:96
	v_lshlrev_b32_e32 v167, 3, v164
	v_xor_b32_e32 v168, 16, v167
	v_sub_u32_e32 v165, v167, v169
	v_sub_u32_e32 v166, v168, v169
	v_add_u32_e32 v172, 0, v165
	v_min_u32_e32 v172, 11, v172
	v_lshlrev_b32_e32 v172, 2, v172
	v_add_u32_e32 v173, 1, v165
	v_min_u32_e32 v173, 11, v173
	v_lshlrev_b32_e32 v173, 2, v173
	v_add_u32_e32 v174, 2, v165
	v_min_u32_e32 v174, 11, v174
	v_lshlrev_b32_e32 v174, 2, v174
	v_add_u32_e32 v175, 3, v165
	v_min_u32_e32 v175, 11, v175
	v_lshlrev_b32_e32 v175, 2, v175
	v_add_u32_e32 v176, 4, v165
	v_min_u32_e32 v176, 11, v176
	v_lshlrev_b32_e32 v176, 2, v176
	v_add_u32_e32 v177, 5, v165
	v_min_u32_e32 v177, 11, v177
	v_lshlrev_b32_e32 v177, 2, v177
	v_add_u32_e32 v178, 6, v165
	v_min_u32_e32 v178, 11, v178
	v_lshlrev_b32_e32 v178, 2, v178
	v_add_u32_e32 v179, 7, v165
	v_min_u32_e32 v179, 11, v179
	v_lshlrev_b32_e32 v179, 2, v179
	v_add_u32_e32 v180, 0, v166
	v_min_u32_e32 v180, 11, v180
	v_lshlrev_b32_e32 v180, 2, v180
	v_add_u32_e32 v181, 1, v166
	v_min_u32_e32 v181, 11, v181
	v_lshlrev_b32_e32 v181, 2, v181
	v_add_u32_e32 v182, 2, v166
	v_min_u32_e32 v182, 11, v182
	v_lshlrev_b32_e32 v182, 2, v182
	v_add_u32_e32 v183, 3, v166
	v_min_u32_e32 v183, 11, v183
	v_lshlrev_b32_e32 v183, 2, v183
	v_add_u32_e32 v184, 4, v166
	v_min_u32_e32 v184, 11, v184
	v_lshlrev_b32_e32 v184, 2, v184
	v_add_u32_e32 v185, 5, v166
	v_min_u32_e32 v185, 11, v185
	v_lshlrev_b32_e32 v185, 2, v185
	v_add_u32_e32 v186, 6, v166
	v_min_u32_e32 v186, 11, v186
	v_lshlrev_b32_e32 v186, 2, v186
	v_add_u32_e32 v187, 7, v166
	v_min_u32_e32 v187, 11, v187
	v_lshlrev_b32_e32 v187, 2, v187
	s_cmp_eq_u32 s15, 7
	s_cselect_b32 s22, 0, 0x20000
	s_add_u32 s84, s18, s22
	s_addc_u32 s85, s19, 0
	s_add_u32 s86, s18, s22
	s_addc_u32 s87, s19, 0
	s_add_u32 s86, s86, 0x1000
	s_addc_u32 s87, s87, 0
	s_add_u32 s88, s20, s22
	s_addc_u32 s89, s21, 0
	s_add_u32 s90, s20, s22
	s_addc_u32 s91, s21, 0
	s_add_u32 s90, s90, 0x1000
	s_addc_u32 s91, s91, 0
	s_waitcnt lgkmcnt(0)
	v_writelane_b32 v171, s40, 0
	v_writelane_b32 v171, s41, 1
	v_writelane_b32 v171, s42, 2
	v_writelane_b32 v171, s43, 3
	v_writelane_b32 v171, s44, 4
	v_writelane_b32 v171, s45, 5
	v_writelane_b32 v171, s46, 6
	v_writelane_b32 v171, s47, 7
	v_writelane_b32 v171, s48, 8
	v_writelane_b32 v171, s49, 9
	v_writelane_b32 v171, s50, 10
	v_writelane_b32 v171, 0, 11
	v_fma_mixlo_f16 v171, v171, s51, 0
	ds_bpermute_b32 v188, v172, v171
	ds_bpermute_b32 v189, v173, v171
	ds_bpermute_b32 v190, v174, v171
	ds_bpermute_b32 v191, v175, v171
	ds_bpermute_b32 v192, v176, v171
	ds_bpermute_b32 v193, v177, v171
	ds_bpermute_b32 v194, v178, v171
	ds_bpermute_b32 v195, v179, v171
	v_mov_b32_e32 v229, 0x44800000
	v_fma_mixlo_f16 v228, s40, v229, 0
	v_cvt_f32_f16_e32 v228, v228
	v_cvt_f64_f32_e32 v[212:213], v228
	v_add_f64 v[212:213], v[212:213], 0
	v_fma_mixlo_f16 v228, s41, v229, 0
	v_cvt_f32_f16_e32 v228, v228
	v_cvt_f64_f32_e32 v[214:215], v228
	v_add_f64 v[212:213], v[212:213], v[214:215]
	v_fma_mixlo_f16 v228, s42, v229, 0
	v_cvt_f32_f16_e32 v228, v228
	v_cvt_f64_f32_e32 v[214:215], v228
	v_add_f64 v[212:213], v[212:213], v[214:215]
	v_fma_mixlo_f16 v228, s43, v229, 0
	v_cvt_f32_f16_e32 v228, v228
	v_cvt_f64_f32_e32 v[214:215], v228
	v_add_f64 v[212:213], v[212:213], v[214:215]
	v_fma_mixlo_f16 v228, s44, v229, 0
	v_cvt_f32_f16_e32 v228, v228
	v_cvt_f64_f32_e32 v[214:215], v228
	v_add_f64 v[212:213], v[212:213], v[214:215]
	v_fma_mixlo_f16 v228, s45, v229, 0
	v_cvt_f32_f16_e32 v228, v228
	v_cvt_f64_f32_e32 v[214:215], v228
	v_add_f64 v[212:213], v[212:213], v[214:215]
	v_fma_mixlo_f16 v228, s46, v229, 0
	v_cvt_f32_f16_e32 v228, v228
	v_cvt_f64_f32_e32 v[214:215], v228
	v_add_f64 v[212:213], v[212:213], v[214:215]
	v_fma_mixlo_f16 v228, s47, v229, 0
	v_cvt_f32_f16_e32 v228, v228
	v_cvt_f64_f32_e32 v[214:215], v228
	v_add_f64 v[212:213], v[212:213], v[214:215]
	v_fma_mixlo_f16 v228, s48, v229, 0
	v_cvt_f32_f16_e32 v228, v228
	v_cvt_f64_f32_e32 v[214:215], v228
	v_add_f64 v[212:213], v[212:213], v[214:215]
	v_fma_mixlo_f16 v228, s49, v229, 0
	v_cvt_f32_f16_e32 v228, v228
	v_cvt_f64_f32_e32 v[214:215], v228
	v_add_f64 v[212:213], v[212:213], v[214:215]
	v_fma_mixlo_f16 v228, s50, v229, 0
	v_cvt_f32_f16_e32 v228, v228
	v_cvt_f64_f32_e32 v[214:215], v228
	v_add_f64 v[212:213], v[212:213], v[214:215]
	s_waitcnt lgkmcnt(7)
	ds_bpermute_b32 v196, v180, v171
	ds_bpermute_b32 v197, v181, v171
	ds_bpermute_b32 v198, v182, v171
	ds_bpermute_b32 v199, v183, v171
	ds_bpermute_b32 v200, v184, v171
	ds_bpermute_b32 v201, v185, v171
	ds_bpermute_b32 v202, v186, v171
	ds_bpermute_b32 v203, v187, v171
	v_mul_f64 v[212:213], v[212:213], v[212:213]
	v_mul_f64 v[216:217], v[212:213], 0.5
	v_add_f64 v[218:219], v[216:217], v[216:217]
	s_mov_b32 s36, 0xeb1c432d
	s_mov_b32 s37, 0x3f1a36e2
	v_mul_f64 v[220:221], v[212:213], s[36:37]
	v_mul_f64 v[222:223], v[216:217], v[218:219]
	v_fmac_f64_e32 v[222:223], v[212:213], v[220:221]
	v_add_f64 v[224:225], v[212:213], v[212:213]
	s_mov_b32 s36, 0x487fcb92
	s_mov_b32 s37, 0x3f4d7dbf
	v_mul_f64 v[226:227], v[212:213], s[36:37]
	v_cvt_f32_f64_e32 v0, v[226:227]
	v_mov_b32_e32 v1, v0
	v_mov_b32_e32 v2, v0
	v_mov_b32_e32 v3, v0
	v_cvt_f32_f64_e32 v10, v[218:219]
	v_cvt_f32_f64_e32 v11, v[222:223]
	v_cvt_f32_f64_e32 v12, v[212:213]
	v_cvt_f32_f64_e32 v13, v[224:225]
	v_mul_f64 v[226:227], v[212:213], v[226:227]
	v_cvt_f32_f64_e32 v14, v[226:227]
	v_lshlrev_b32_e32 v167, 2, v164
	s_cmp_eq_u32 s12, 0
	s_cselect_b32 s23, 6, 64
	v_add_u32_e32 v168, 0, v167
	v_cmp_gt_u32_e32 vcc, s23, v168
	s_nop 1
	v_cndmask_b32_e64 v15, 0, 1.0, vcc
	v_add_u32_e32 v168, 1, v167
	v_cmp_gt_u32_e32 vcc, s23, v168
	s_nop 1
	v_cndmask_b32_e64 v16, 0, 1.0, vcc
	v_add_u32_e32 v168, 2, v167
	v_cmp_gt_u32_e32 vcc, s23, v168
	s_nop 1
	v_cndmask_b32_e64 v17, 0, 1.0, vcc
	v_add_u32_e32 v168, 3, v167
	v_cmp_gt_u32_e32 vcc, s23, v168
	s_nop 1
	v_cndmask_b32_e64 v18, 0, 1.0, vcc
	v_and_b32_e32 v167, 31, v8
	v_lshlrev_b32_e32 v167, 4, v167
	s_lshl_b32 s24, s12, 11
	s_add_i32 s25, s12, 7
	s_and_b32 s25, s25, 7
	s_lshl_b32 s26, s25, 11
	v_or_b32_e32 v4, s24, v167
	v_or_b32_e32 v5, s26, v167
	s_lshl_b32 s28, s25, 2
	s_add_u32 s28, s28, 0x10000
	v_mov_b32_e32 v7, s28
	v_mov_b32_e32 v19, 0
	v_mov_b32_e32 v20, 0
	v_mov_b32_e32 v21, 0
	v_mov_b32_e32 v22, 0
	s_waitcnt lgkmcnt(0)
	v_cmp_lt_u32_e64 s[32:33], 31, v8
	v_cmp_gt_u32_e64 s[34:35], 32, v8
	v_pack_b32_f16 v24, v188, v189
	v_pack_b32_f16 v25, v190, v191
	v_pack_b32_f16 v26, v192, v193
	v_pack_b32_f16 v27, v194, v195
	v_pack_b32_f16 v167, v196, v197
	v_cndmask_b32_e64 v28, 0, v167, s[32:33]
	v_cndmask_b32_e64 v32, 0, v167, s[34:35]
	v_pack_b32_f16 v167, v198, v199
	v_cndmask_b32_e64 v29, 0, v167, s[32:33]
	v_cndmask_b32_e64 v33, 0, v167, s[34:35]
	v_pack_b32_f16 v167, v200, v201
	v_cndmask_b32_e64 v30, 0, v167, s[32:33]
	v_cndmask_b32_e64 v34, 0, v167, s[34:35]
	v_pack_b32_f16 v167, v202, v203
	v_cndmask_b32_e64 v31, 0, v167, s[32:33]
	v_cndmask_b32_e64 v35, 0, v167, s[34:35]
	s_waitcnt lgkmcnt(0)
	s_barrier
	s_cmp_lt_u32 s12, 4
	s_cbranch_scc1 .Lq_noprio
	s_setprio 1
.Lq_noprio:
	s_waitcnt vmcnt(12)
	v_cvt_pk_f16_f32 v164, v36, v40
	v_cvt_pk_f16_f32 v180, v68, v72
	v_pk_add_f16 v164, v164, -0.5 op_sel_hi:[1,0]
	v_pk_add_f16 v180, v180, -0.5 op_sel_hi:[1,0]
	v_pk_mul_f16 v196, v180, v180
	v_pk_mul_f16 v212, v164, v180
	v_pk_fma_f16 v196, v164, v164, v196
	v_cvt_pk_f16_f32 v168, v37, v41
	v_cvt_pk_f16_f32 v184, v69, v73
	v_pk_add_f16 v168, v168, -0.5 op_sel_hi:[1,0]
	v_pk_add_f16 v184, v184, -0.5 op_sel_hi:[1,0]
	v_pk_mul_f16 v200, v184, v184
	v_pk_mul_f16 v216, v168, v184
	v_pk_fma_f16 v200, v168, v168, v200
	v_cvt_pk_f16_f32 v172, v38, v42
	v_cvt_pk_f16_f32 v188, v70, v74
	v_pk_add_f16 v172, v172, -0.5 op_sel_hi:[1,0]
	v_pk_add_f16 v188, v188, -0.5 op_sel_hi:[1,0]
	v_pk_mul_f16 v204, v188, v188
	v_pk_mul_f16 v220, v172, v188
	v_pk_fma_f16 v204, v172, v172, v204
	v_cvt_pk_f16_f32 v176, v39, v43
	v_cvt_pk_f16_f32 v192, v71, v75
	v_pk_add_f16 v176, v176, -0.5 op_sel_hi:[1,0]
	v_pk_add_f16 v192, v192, -0.5 op_sel_hi:[1,0]
	v_pk_mul_f16 v208, v192, v192
	v_pk_mul_f16 v224, v176, v192
	v_pk_fma_f16 v208, v176, v176, v208
	s_waitcnt vmcnt(8)
	v_cvt_pk_f16_f32 v165, v44, v48
	v_cvt_pk_f16_f32 v181, v76, v80
	v_pk_add_f16 v165, v165, -0.5 op_sel_hi:[1,0]
	v_pk_add_f16 v181, v181, -0.5 op_sel_hi:[1,0]
	v_pk_mul_f16 v197, v181, v181
	v_pk_mul_f16 v213, v165, v181
	v_pk_fma_f16 v197, v165, v165, v197
	v_cvt_pk_f16_f32 v169, v45, v49
	v_cvt_pk_f16_f32 v185, v77, v81
	v_pk_add_f16 v169, v169, -0.5 op_sel_hi:[1,0]
	v_pk_add_f16 v185, v185, -0.5 op_sel_hi:[1,0]
	v_pk_mul_f16 v201, v185, v185
	v_pk_mul_f16 v217, v169, v185
	v_pk_fma_f16 v201, v169, v169, v201
	v_cvt_pk_f16_f32 v173, v46, v50
	v_cvt_pk_f16_f32 v189, v78, v82
	v_pk_add_f16 v173, v173, -0.5 op_sel_hi:[1,0]
	v_pk_add_f16 v189, v189, -0.5 op_sel_hi:[1,0]
	v_pk_mul_f16 v205, v189, v189
	v_pk_mul_f16 v221, v173, v189
	v_pk_fma_f16 v205, v173, v173, v205
	v_cvt_pk_f16_f32 v177, v47, v51
	v_cvt_pk_f16_f32 v193, v79, v83
	v_pk_add_f16 v177, v177, -0.5 op_sel_hi:[1,0]
	v_pk_add_f16 v193, v193, -0.5 op_sel_hi:[1,0]
	v_pk_mul_f16 v209, v193, v193
	v_pk_mul_f16 v225, v177, v193
	v_pk_fma_f16 v209, v177, v177, v209
	s_waitcnt vmcnt(4)
	v_cvt_pk_f16_f32 v166, v52, v56
	v_cvt_pk_f16_f32 v182, v84, v88
	v_pk_add_f16 v166, v166, -0.5 op_sel_hi:[1,0]
	v_pk_add_f16 v182, v182, -0.5 op_sel_hi:[1,0]
	v_pk_mul_f16 v198, v182, v182
	v_pk_mul_f16 v214, v166, v182
	v_pk_fma_f16 v198, v166, v166, v198
	v_cvt_pk_f16_f32 v170, v53, v57
	v_cvt_pk_f16_f32 v186, v85, v89
	v_pk_add_f16 v170, v170, -0.5 op_sel_hi:[1,0]
	v_pk_add_f16 v186, v186, -0.5 op_sel_hi:[1,0]
	v_pk_mul_f16 v202, v186, v186
	v_pk_mul_f16 v218, v170, v186
	v_pk_fma_f16 v202, v170, v170, v202
	v_cvt_pk_f16_f32 v174, v54, v58
	v_cvt_pk_f16_f32 v190, v86, v90
	v_pk_add_f16 v174, v174, -0.5 op_sel_hi:[1,0]
	v_pk_add_f16 v190, v190, -0.5 op_sel_hi:[1,0]
	v_pk_mul_f16 v206, v190, v190
	v_pk_mul_f16 v222, v174, v190
	v_pk_fma_f16 v206, v174, v174, v206
	v_cvt_pk_f16_f32 v178, v55, v59
	v_cvt_pk_f16_f32 v194, v87, v91
	v_pk_add_f16 v178, v178, -0.5 op_sel_hi:[1,0]
	v_pk_add_f16 v194, v194, -0.5 op_sel_hi:[1,0]
	v_pk_mul_f16 v210, v194, v194
	v_pk_mul_f16 v226, v178, v194
	v_pk_fma_f16 v210, v178, v178, v210
	s_waitcnt vmcnt(0)
	v_cvt_pk_f16_f32 v167, v60, v64
	v_cvt_pk_f16_f32 v183, v92, v96
	v_pk_add_f16 v167, v167, -0.5 op_sel_hi:[1,0]
	v_pk_add_f16 v183, v183, -0.5 op_sel_hi:[1,0]
	v_pk_mul_f16 v199, v183, v183
	v_pk_mul_f16 v215, v167, v183
	v_pk_fma_f16 v199, v167, v167, v199
	v_cvt_pk_f16_f32 v171, v61, v65
	v_cvt_pk_f16_f32 v187, v93, v97
	v_pk_add_f16 v171, v171, -0.5 op_sel_hi:[1,0]
	v_pk_add_f16 v187, v187, -0.5 op_sel_hi:[1,0]
	v_pk_mul_f16 v203, v187, v187
	v_pk_mul_f16 v219, v171, v187
	v_pk_fma_f16 v203, v171, v171, v203
	v_cvt_pk_f16_f32 v175, v62, v66
	v_cvt_pk_f16_f32 v191, v94, v98
	v_pk_add_f16 v175, v175, -0.5 op_sel_hi:[1,0]
	v_pk_add_f16 v191, v191, -0.5 op_sel_hi:[1,0]
	v_pk_mul_f16 v207, v191, v191
	v_pk_mul_f16 v223, v175, v191
	v_pk_fma_f16 v207, v175, v175, v207
	v_cvt_pk_f16_f32 v179, v63, v67
	v_cvt_pk_f16_f32 v195, v95, v99
	v_pk_add_f16 v179, v179, -0.5 op_sel_hi:[1,0]
	v_pk_add_f16 v195, v195, -0.5 op_sel_hi:[1,0]
	v_pk_mul_f16 v211, v195, v195
	v_pk_mul_f16 v227, v179, v195
	v_pk_fma_f16 v211, v179, v179, v211
	global_load_dwordx4 v[100:103], v240, s[18:19] offset:0 nt
	global_load_dwordx4 v[104:107], v240, s[18:19] offset:2048 nt
	global_load_dwordx4 v[132:135], v240, s[20:21] offset:0 nt
	global_load_dwordx4 v[136:139], v240, s[20:21] offset:2048 nt
	global_load_dwordx4 v[108:111], v241, s[18:19] offset:0 nt
	global_load_dwordx4 v[112:115], v241, s[18:19] offset:2048 nt
	global_load_dwordx4 v[140:143], v241, s[20:21] offset:0 nt
	global_load_dwordx4 v[144:147], v241, s[20:21] offset:2048 nt
	global_load_dwordx4 v[116:119], v242, s[18:19] offset:0 nt
	global_load_dwordx4 v[120:123], v242, s[18:19] offset:2048 nt
	global_load_dwordx4 v[148:151], v242, s[20:21] offset:0 nt
	global_load_dwordx4 v[152:155], v242, s[20:21] offset:2048 nt
	global_load_dwordx4 v[124:127], v243, s[18:19] offset:0 nt
	global_load_dwordx4 v[128:131], v243, s[18:19] offset:2048 nt
	global_load_dwordx4 v[156:159], v243, s[20:21] offset:0 nt
	global_load_dwordx4 v[160:163], v243, s[20:21] offset:2048 nt
	v_mfma_f32_16x16x32_f16 v[68:71], v[164:167], v[24:27], 0
	v_mfma_f32_16x16x32_f16 v[72:75], v[168:171], v[24:27], 0
	v_mfma_f32_16x16x32_f16 v[76:79], v[172:175], v[24:27], 0
	v_mfma_f32_16x16x32_f16 v[80:83], v[176:179], v[24:27], 0
	v_mfma_f32_16x16x32_f16 v[84:87], v[180:183], v[24:27], 0
	v_mfma_f32_16x16x32_f16 v[88:91], v[184:187], v[24:27], 0
	v_mfma_f32_16x16x32_f16 v[92:95], v[188:191], v[24:27], 0
	v_mfma_f32_16x16x32_f16 v[96:99], v[192:195], v[24:27], 0
	s_nop 1
	v_cvt_pk_f16_f32 v36, v68, v72
	s_nop 0
	v_cvt_pk_f16_f32 v37, v76, v80
	v_cvt_pk_f16_f32 v38, v69, v73
	v_cvt_pk_f16_f32 v39, v77, v81
	v_cvt_pk_f16_f32 v40, v70, v74
	v_cvt_pk_f16_f32 v41, v78, v82
	v_cvt_pk_f16_f32 v42, v71, v75
	v_cvt_pk_f16_f32 v43, v79, v83
	v_mfma_f32_16x16x32_f16 v[68:71], v[196:199], v[24:27], 0
	v_mfma_f32_16x16x32_f16 v[72:75], v[200:203], v[24:27], 0
	v_mfma_f32_16x16x32_f16 v[76:79], v[204:207], v[24:27], 0
	v_mfma_f32_16x16x32_f16 v[80:83], v[208:211], v[24:27], 0
	v_cvt_pk_f16_f32 v44, v84, v88
	v_cvt_pk_f16_f32 v45, v92, v96
	v_cvt_pk_f16_f32 v46, v85, v89
	v_cvt_pk_f16_f32 v47, v93, v97
	v_cvt_pk_f16_f32 v48, v86, v90
	v_cvt_pk_f16_f32 v49, v94, v98
	v_cvt_pk_f16_f32 v50, v87, v91
	v_cvt_pk_f16_f32 v51, v95, v99
	v_mfma_f32_16x16x32_f16 v[84:87], v[212:215], v[24:27], 0
	v_mfma_f32_16x16x32_f16 v[88:91], v[216:219], v[24:27], 0
	v_mfma_f32_16x16x32_f16 v[92:95], v[220:223], v[24:27], 0
	v_mfma_f32_16x16x32_f16 v[96:99], v[224:227], v[24:27], 0
	v_cvt_pk_f16_f32 v52, v68, v72
	v_cvt_pk_f16_f32 v53, v76, v80
	v_cvt_pk_f16_f32 v54, v69, v73
	v_cvt_pk_f16_f32 v55, v77, v81
	v_cvt_pk_f16_f32 v56, v70, v74
	v_cvt_pk_f16_f32 v57, v78, v82
	v_cvt_pk_f16_f32 v58, v71, v75
	v_cvt_pk_f16_f32 v59, v79, v83
	v_cvt_pk_f16_f32 v60, v84, v88
	v_cvt_pk_f16_f32 v61, v92, v96
	v_cvt_pk_f16_f32 v62, v85, v89
	v_cvt_pk_f16_f32 v63, v93, v97
	v_cvt_pk_f16_f32 v64, v86, v90
	v_cvt_pk_f16_f32 v65, v94, v98
	v_cvt_pk_f16_f32 v66, v87, v91
	v_cvt_pk_f16_f32 v67, v95, v99
	s_mov_b64 exec, s[38:39]
	ds_write_b128 v4, v[40:43] offset:0
	ds_write_b128 v4, v[48:51] offset:512
	ds_write_b128 v4, v[56:59] offset:1024
	ds_write_b128 v4, v[64:67] offset:1536
	s_mov_b64 exec, -1
	v_mfma_f32_16x16x32_f16 v[68:71], v[24:27], v[36:39], 0
	v_mfma_f32_16x16x32_f16 v[72:75], v[24:27], v[44:47], 0
	v_mfma_f32_16x16x32_f16 v[76:79], v[24:27], v[52:55], v[0:3]
	v_mfma_f32_16x16x32_f16 v[80:83], v[24:27], v[60:63], 0
	v_mfma_f32_16x16x32_f16 v[84:87], v[28:31], v[36:39], 0
	v_mfma_f32_16x16x32_f16 v[88:91], v[28:31], v[44:47], 0
	v_mfma_f32_16x16x32_f16 v[92:95], v[28:31], v[52:55], v[0:3]
	v_mfma_f32_16x16x32_f16 v[96:99], v[28:31], v[60:63], 0
	v_mfma_f32_16x16x32_f16 v[84:87], v[32:35], v[40:43], v[84:87]
	v_mfma_f32_16x16x32_f16 v[88:91], v[32:35], v[48:51], v[88:91]
	v_mfma_f32_16x16x32_f16 v[92:95], v[32:35], v[56:59], v[92:95]
	v_mfma_f32_16x16x32_f16 v[96:99], v[32:35], v[64:67], v[96:99]
	s_waitcnt lgkmcnt(0)
	ds_write_b32 v6, v6 offset:0
	ds_read_b32 v9, v7 offset:0
	v_mul_f32_e32 v244, v68, v72
	v_mul_f32_e32 v250, v69, v73
	v_mul_f32_e64 v245, -v72, v72
	v_mul_f32_e64 v251, -v73, v73
	v_add_f32_e32 v246, v68, v72
	v_add_f32_e32 v252, v69, v73
	v_fma_f32 v245, -v68, v68, v245
	v_fma_f32 v251, -v69, v69, v251
	v_fma_f32 v247, v10, v246, v11
	v_fma_f32 v253, v10, v252, v11
	v_fma_f32 v246, v13, v80, v14
	v_fma_f32 v252, v13, v81, v14
	v_fma_f32 v248, v12, v76, v245
	v_fma_f32 v254, v12, v77, v251
	v_fma_f32 v249, 2.0, v244, v247
	v_fma_f32 v255, 2.0, v250, v253
	v_sub_f32_e32 v247, v247, v245
	v_sub_f32_e32 v253, v253, v251
	v_fma_f32 v246, -2.0, v244, v246
	v_fma_f32 v252, -2.0, v250, v252
	v_mul_f32_e32 v247, v247, v248
	v_mul_f32_e32 v253, v253, v254
	v_rcp_f32_e32 v247, v247
	v_rcp_f32_e32 v253, v253
	v_mul_f32_e32 v249, v249, v246
	v_mul_f32_e32 v255, v255, v252
	v_fma_f32 v19, v249, v247, v19
	v_fma_f32 v19, v255, v253, v19
	v_mul_f32_e32 v244, v70, v74
	v_mul_f32_e32 v250, v71, v75
	v_mul_f32_e64 v245, -v74, v74
	v_mul_f32_e64 v251, -v75, v75
	v_add_f32_e32 v246, v70, v74
	v_add_f32_e32 v252, v71, v75
	v_fma_f32 v245, -v70, v70, v245
	v_fma_f32 v251, -v71, v71, v251
	v_fma_f32 v247, v10, v246, v11
	v_fma_f32 v253, v10, v252, v11
	v_fma_f32 v246, v13, v82, v14
	v_fma_f32 v252, v13, v83, v14
	v_fma_f32 v248, v12, v78, v245
	v_fma_f32 v254, v12, v79, v251
	v_fma_f32 v249, 2.0, v244, v247
	v_fma_f32 v255, 2.0, v250, v253
	v_sub_f32_e32 v247, v247, v245
	v_sub_f32_e32 v253, v253, v251
	v_fma_f32 v246, -2.0, v244, v246
	v_fma_f32 v252, -2.0, v250, v252
	v_mul_f32_e32 v247, v247, v248
	v_mul_f32_e32 v253, v253, v254
	v_rcp_f32_e32 v247, v247
	v_rcp_f32_e32 v253, v253
	v_mul_f32_e32 v249, v249, v246
	v_mul_f32_e32 v255, v255, v252
	v_fma_f32 v20, v249, v247, v20
	v_fma_f32 v20, v255, v253, v20
	v_mfma_f32_16x16x32_f16 v[68:71], v[24:27], v[40:43], 0
	v_mfma_f32_16x16x32_f16 v[72:75], v[24:27], v[48:51], 0
	v_mfma_f32_16x16x32_f16 v[76:79], v[24:27], v[56:59], v[0:3]
	v_mfma_f32_16x16x32_f16 v[80:83], v[24:27], v[64:67], 0
	s_waitcnt lgkmcnt(0)
	v_cmp_ne_u32_e32 vcc, 0, v9
	s_cbranch_vccnz .Lq_go_0
